# attention loop: counted lgkmcnt waits, each MFMA waits only for its own fragment reads
# speedup vs baseline: 1.0040x; 1.0008x over previous
; __device__ __forceinline__ void partialSM(f32x16& p0, f32x16& p1, float& m_reg, float& alpha, const bool first) {
;     float ma = max3f(p0[0], p0[1], p0[2]), mb = max3f(p0[3], p0[4], p0[5]), mc = max3f(p0[6], p0[7], p0[8]), md = max3f(p0[9], p0[10], p0[11]);
;     ma = max3f(ma, p0[12], p0[13]); mb = max3f(mb, p0[14], p0[15]); mc = max3f(mc, p1[0], p1[1]); md = max3f(md, p1[2], p1[3]);
;     ma = max3f(ma, p1[4], p1[5]); mb = max3f(mb, p1[6], p1[7]); mc = max3f(mc, p1[8], p1[9]); md = max3f(md, p1[10], p1[11]);
;     ma = max3f(ma, p1[12], p1[13]); mb = max3f(mb, p1[14], p1[15]);
;     float pmax = fmaxf(max3f(ma, mb, mc), md);
;     { auto rr = __builtin_amdgcn_permlane32_swap(__float_as_uint(pmax), __float_as_uint(pmax), false, false);
;       pmax = fmaxf(__uint_as_float(rr[0]), __uint_as_float(rr[1])); }
;     const float u = pmax - PSH;
;     if (__builtin_expect(!first && __all(u <= THR2), 1)) { alpha = 1.f; }
;     else { const float dl = first ? u : fmaxf(u, 0.f); alpha = __builtin_amdgcn_exp2f(-dl); m_reg += dl;
; #pragma unroll
;         for (int r = 0; r < 16; ++r) { p0[r] -= dl; p1[r] -= dl; } }
; #pragma unroll
;     for (int r = 0; r < 16; ++r) p0[r] = __builtin_amdgcn_exp2f(p0[r]);
; }
; __device__ __forceinline__ void finishSM(f32x16& p0, f32x16& p1, float alpha, float& l_reg, v8i& pa) {
; #pragma unroll
;     for (int r = 0; r < 16; ++r) p1[r] = __builtin_amdgcn_exp2f(p1[r]);
;     float sa = p0[0] + p0[1], sb = p0[2] + p0[3], sc = p0[4] + p0[5], sd = p0[6] + p0[7];
;     sa += p0[8]; sb += p0[9]; sc += p0[10]; sd += p0[11]; sa += p0[12]; sb += p0[13]; sc += p0[14]; sd += p0[15];
; #pragma unroll
;     for (int r = 0; r < 16; r += 4) { sa += p1[r]; sb += p1[r + 1]; sc += p1[r + 2]; sd += p1[r + 3]; }
;     float ps = (sa + sb) + (sc + sd);
;     { auto rr = __builtin_amdgcn_permlane32_swap(__float_as_uint(ps), __float_as_uint(ps), false, false);
;       ps = __uint_as_float(rr[0]) + __uint_as_float(rr[1]); }
;     l_reg = l_reg * alpha + ps;
; #pragma unroll
;     for (int c = 0; c < 4; ++c) { pa[c] = (int)pk4_fp8(p0[4 * c], p0[4 * c + 1], p0[4 * c + 2], p0[4 * c + 3]);
;         pa[4 + c] = (int)pk4_fp8(p1[4 * c], p1[4 * c + 1], p1[4 * c + 2], p1[4 * c + 3]); }
; }
; __device__ __forceinline__ void qkt(f32x16& p0, f32x16& p1, const float m_reg, const char* Ks, const v8i* q8, int r32, int hi) {
;     { const float ini = PSH - m_reg;
.LBB0_553:
	v_sub_f32_e32 v80, 0x40400000, v180
	v_mov_b32_e32 v81, v80
	v_mov_b64_e32 v[82:83], v[80:81]
	v_mov_b64_e32 v[84:85], v[80:81]
	v_mov_b64_e32 v[86:87], v[80:81]
	v_mov_b64_e32 v[88:89], v[80:81]
	v_mov_b64_e32 v[90:91], v[80:81]
	v_mov_b64_e32 v[92:93], v[80:81]
	v_mov_b64_e32 v[94:95], v[80:81]
	v_exp_f32_e32 v228, v64
	v_exp_f32_e32 v230, v65
	s_waitcnt lgkmcnt(2)
	v_mfma_scale_f32_32x32x64_f8f6f4 v[96:111], v[96:103], v[120:127], v[80:95], v201, v200 op_sel_hi:[0,0,0]
	v_exp_f32_e32 v222, v66
	v_exp_f32_e32 v223, v67
	v_exp_f32_e32 v229, v68
	v_exp_f32_e32 v231, v69
	v_exp_f32_e32 v226, v70
	v_exp_f32_e32 v227, v71
	v_add_f32_e32 v64, v215, v216
	v_add_f32_e32 v65, v190, v192
	v_add_f32_e32 v66, v213, v214
	v_add_f32_e32 v67, v195, v212
	v_exp_f32_e32 v224, v72
	v_exp_f32_e32 v225, v73
	v_exp_f32_e32 v184, v74
	v_exp_f32_e32 v217, v75
	v_add_f32_e32 v64, v194, v64
	s_waitcnt lgkmcnt(0)
	v_mfma_scale_f32_32x32x64_f8f6f4 v[80:95], v[136:143], v[120:127], v[80:95], v201, v200 op_sel_hi:[0,0,0]
	ds_read_b128 v[136:139], v164 offset:64
	ds_read_b128 v[140:143], v164 offset:80
	ds_read_b128 v[144:147], v164 offset:6720
	ds_read_b128 v[148:151], v164 offset:6736
	v_add_f32_e32 v65, v211, v65
	v_add_f32_e32 v66, v186, v66
	v_add_f32_e32 v67, v187, v67
	v_exp_f32_e32 v220, v76
	v_exp_f32_e32 v221, v77
	v_exp_f32_e32 v218, v78
	v_exp_f32_e32 v219, v79
	v_add_f32_e32 v64, v191, v64
	v_add_f32_e32 v65, v193, v65
	v_add_f32_e32 v66, v188, v66
	v_add_f32_e32 v67, v189, v67
	v_add_f32_e32 v64, v228, v64
	v_add_f32_e32 v65, v230, v65
	v_add_f32_e32 v66, v222, v66
	s_waitcnt lgkmcnt(2)
	v_mfma_scale_f32_32x32x64_f8f6f4 v[96:111], v[136:143], v[128:135], v[96:111], v201, v200 op_sel_hi:[0,0,0]
	v_add_f32_e32 v67, v223, v67
	v_add_f32_e32 v64, v229, v64
	v_add_f32_e32 v65, v231, v65
	v_add_f32_e32 v66, v226, v66
	v_add_f32_e32 v67, v227, v67
	v_add_f32_e32 v64, v224, v64
	v_add_f32_e32 v65, v225, v65
	v_add_f32_e32 v66, v184, v66
	v_add_f32_e32 v67, v217, v67
	v_add_f32_e32 v64, v220, v64
	v_add_f32_e32 v65, v221, v65
	v_add_f32_e32 v66, v218, v66
	v_add_f32_e32 v67, v219, v67
	v_add_f32_e32 v64, v65, v64
	v_add_f32_e32 v65, v66, v67
	s_waitcnt lgkmcnt(0)
	v_mfma_scale_f32_32x32x64_f8f6f4 v[80:95], v[144:151], v[128:135], v[80:95], v201, v200 op_sel_hi:[0,0,0]
	ds_read_b128 v[136:139], v164 offset:128
	ds_read_b128 v[140:143], v164 offset:144
	ds_read_b128 v[144:147], v164 offset:6784
	ds_read_b128 v[148:151], v164 offset:6800
	v_add_f32_e32 v182, v65, v64
	v_mov_b32_e32 v183, v182
	v_cvt_pk_fp8_f32 v232, v215, v216
	v_cvt_pk_fp8_f32 v236, v228, v230
	v_cvt_pk_fp8_f32 v233, v213, v214
	v_cvt_pk_fp8_f32 v237, v229, v231
	v_cvt_pk_fp8_f32 v234, v194, v211
	v_cvt_pk_fp8_f32 v238, v224, v225
	v_cvt_pk_fp8_f32 v235, v191, v193
	v_cvt_pk_fp8_f32 v239, v220, v221
	v_permlane32_swap_b32_e32 v182, v183
	s_waitcnt lgkmcnt(2)
	v_mfma_scale_f32_32x32x64_f8f6f4 v[96:111], v[136:143], v[112:119], v[96:111], v201, v200 op_sel_hi:[0,0,0]
	v_cvt_pk_fp8_f32 v232, v190, v192 op_sel:[0,0,1]
	v_cvt_pk_fp8_f32 v236, v222, v223 op_sel:[0,0,1]
	v_cvt_pk_fp8_f32 v233, v195, v212 op_sel:[0,0,1]
	v_cvt_pk_fp8_f32 v237, v226, v227 op_sel:[0,0,1]
	v_cvt_pk_fp8_f32 v234, v186, v187 op_sel:[0,0,1]
	v_cvt_pk_fp8_f32 v238, v184, v217 op_sel:[0,0,1]
	v_cvt_pk_fp8_f32 v235, v188, v189 op_sel:[0,0,1]
	v_cvt_pk_fp8_f32 v239, v218, v219 op_sel:[0,0,1]
	s_waitcnt lgkmcnt(0)
	v_mfma_scale_f32_32x32x64_f8f6f4 v[80:95], v[144:151], v[112:119], v[80:95], v201, v200 op_sel_hi:[0,0,0]
	s_mul_i32 s15, s10, 0x5c00
	s_add_i32 s11, s15, 0
	v_add_u32_e32 v64, s11, v161
	v_add_u32_e32 v176, v64, v179
	ds_read_b128 v[144:147], v176 offset:13312
	ds_read_b128 v[148:151], v176 offset:13328
	ds_read_b128 v[136:139], v176 offset:15872
	ds_read_b128 v[140:143], v176 offset:15888
	ds_read_b128 v[72:75], v176 offset:18432
	ds_read_b128 v[76:79], v176 offset:18448
	ds_read_b128 v[64:67], v176 offset:20992
	ds_read_b128 v[68:71], v176 offset:21008
	v_max_f32_e32 v164, v96, v97
	v_max3_f32 v165, v99, v100, v101
	v_max3_f32 v164, v164, v98, v108
	v_max3_f32 v165, v165, v110, v111
	v_max3_f32 v166, v102, v103, v104
	v_max3_f32 v167, v105, v106, v107
	s_waitcnt lgkmcnt(6)
	v_mfma_scale_f32_32x32x64_f8f6f4 v[0:15], v[232:239], v[144:151], v[0:15], v201, v201 op_sel_hi:[0,0,0]
	v_max3_f32 v164, v164, v109, v84
	v_max3_f32 v165, v165, v86, v87
	v_max3_f32 v166, v166, v80, v81
	v_max3_f32 v167, v167, v82, v83
	v_max3_f32 v164, v164, v85, v92
	v_max3_f32 v165, v165, v94, v95
	v_max3_f32 v166, v166, v88, v89
	v_max3_f32 v167, v167, v90, v91
	s_waitcnt lgkmcnt(4)
	v_mfma_scale_f32_32x32x64_f8f6f4 v[48:63], v[232:239], v[136:143], v[48:63], v201, v201 op_sel_hi:[0,0,0]
	v_max3_f32 v164, v164, v93, v165
	v_max3_f32 v164, v164, v166, v167
	s_mov_b32 s0, 0x410c551d
	v_cmp_ge_f32_e32 vcc, s0, v164
	s_cmp_eq_u64 vcc, exec
	v_mov_b32_e32 v185, 1.0
	s_cbranch_scc0 .LBB0_570
; __device__ __forceinline__ void partialSM(f32x16& p0, f32x16& p1, float& m_reg, float& alpha, const bool first) {
;     ...
;     if (__builtin_expect(!first && __all(u <= THR2), 1)) { alpha = 1.f; }
;     else { const float dl = first ? u : fmaxf(u, 0.f); alpha = __builtin_amdgcn_exp2f(-dl); m_reg += dl;
; #pragma unroll
;         for (int r = 0; r < 16; ++r) { p0[r] -= dl; p1[r] -= dl; } }
; #pragma unroll
;     for (int r = 0; r < 16; ++r) p0[r] = __builtin_amdgcn_exp2f(p0[r]);
.LBB0_554:
	s_waitcnt lgkmcnt(2)
	v_mfma_scale_f32_32x32x64_f8f6f4 v[32:47], v[232:239], v[72:79], v[32:47], v201, v201 op_sel_hi:[0,0,0]
	v_exp_f32_e32 v215, v96
	v_exp_f32_e32 v216, v97
	v_exp_f32_e32 v192, v98
	v_exp_f32_e32 v194, v99
	v_exp_f32_e32 v213, v100
	v_exp_f32_e32 v214, v101
	v_exp_f32_e32 v211, v102
	v_exp_f32_e32 v212, v103
	s_waitcnt lgkmcnt(0)
	v_mfma_scale_f32_32x32x64_f8f6f4 v[16:31], v[232:239], v[64:71], v[16:31], v201, v201 op_sel_hi:[0,0,0]
	v_cmp_gt_f32_e32 vcc, 1.0, v185
	v_exp_f32_e32 v193, v104
	v_exp_f32_e32 v195, v105
	v_exp_f32_e32 v186, v106
	v_exp_f32_e32 v187, v107
	v_exp_f32_e32 v190, v108
	v_exp_f32_e32 v191, v109
	v_exp_f32_e32 v188, v110
	v_exp_f32_e32 v189, v111
	s_cbranch_vccz .LBB0_558
	s_and_saveexec_b64 s[0:1], s[44:45]
	ds_write_b32 v174, v185 offset:128
	s_or_b64 exec, exec, s[0:1]
	s_waitcnt lgkmcnt(0)
	v_add_u32_e32 v76, s31, v173
	ds_read_b128 v[64:67], v76 offset:224
	ds_read_b128 v[68:71], v76 offset:192
	ds_read_b128 v[72:75], v76 offset:160
	ds_read_b128 v[76:79], v76 offset:128
	s_waitcnt lgkmcnt(0)
	s_nop 6
	v_pk_mul_f32 v[12:13], v[12:13], v[64:65]
	v_pk_mul_f32 v[8:9], v[8:9], v[68:69]
	v_pk_mul_f32 v[4:5], v[4:5], v[72:73]
	v_pk_mul_f32 v[14:15], v[14:15], v[66:67]
	v_pk_mul_f32 v[10:11], v[10:11], v[70:71]
	v_pk_mul_f32 v[6:7], v[6:7], v[74:75]
	v_pk_mul_f32 v[2:3], v[2:3], v[78:79]
	v_pk_mul_f32 v[0:1], v[0:1], v[76:77]
	v_pk_mul_f32 v[60:61], v[60:61], v[64:65]
	v_pk_mul_f32 v[56:57], v[56:57], v[68:69]
	v_pk_mul_f32 v[52:53], v[52:53], v[72:73]
	v_pk_mul_f32 v[62:63], v[62:63], v[66:67]
	v_pk_mul_f32 v[58:59], v[58:59], v[70:71]
	v_pk_mul_f32 v[54:55], v[54:55], v[74:75]
	v_pk_mul_f32 v[50:51], v[50:51], v[78:79]
	v_pk_mul_f32 v[48:49], v[48:49], v[76:77]
	v_pk_mul_f32 v[44:45], v[44:45], v[64:65]
	v_pk_mul_f32 v[40:41], v[40:41], v[68:69]
	v_pk_mul_f32 v[36:37], v[36:37], v[72:73]
	v_pk_mul_f32 v[46:47], v[46:47], v[66:67]
	v_pk_mul_f32 v[42:43], v[42:43], v[70:71]
	v_pk_mul_f32 v[38:39], v[38:39], v[74:75]
	v_pk_mul_f32 v[34:35], v[34:35], v[78:79]
	v_pk_mul_f32 v[32:33], v[32:33], v[76:77]
	v_pk_mul_f32 v[28:29], v[28:29], v[64:65]
	v_pk_mul_f32 v[24:25], v[24:25], v[68:69]
	v_pk_mul_f32 v[20:21], v[20:21], v[72:73]
	v_pk_mul_f32 v[30:31], v[30:31], v[66:67]
	v_pk_mul_f32 v[26:27], v[26:27], v[70:71]
	v_pk_mul_f32 v[22:23], v[22:23], v[74:75]
	v_pk_mul_f32 v[18:19], v[18:19], v[78:79]
	v_pk_mul_f32 v[16:17], v[16:17], v[76:77]

; __device__ __forceinline__ void partialSM(f32x16& p0, f32x16& p1, float& m_reg, float& alpha, const bool first) {
;     float ma = max3f(p0[0], p0[1], p0[2]), mb = max3f(p0[3], p0[4], p0[5]), mc = max3f(p0[6], p0[7], p0[8]), md = max3f(p0[9], p0[10], p0[11]);
;     ma = max3f(ma, p0[12], p0[13]); mb = max3f(mb, p0[14], p0[15]); mc = max3f(mc, p1[0], p1[1]); md = max3f(md, p1[2], p1[3]);
;     ma = max3f(ma, p1[4], p1[5]); mb = max3f(mb, p1[6], p1[7]); mc = max3f(mc, p1[8], p1[9]); md = max3f(md, p1[10], p1[11]);
;     ma = max3f(ma, p1[12], p1[13]); mb = max3f(mb, p1[14], p1[15]);
;     float pmax = fmaxf(max3f(ma, mb, mc), md);
;     { auto rr = __builtin_amdgcn_permlane32_swap(__float_as_uint(pmax), __float_as_uint(pmax), false, false);
;       pmax = fmaxf(__uint_as_float(rr[0]), __uint_as_float(rr[1])); }
;     const float u = pmax - PSH;
;     if (__builtin_expect(!first && __all(u <= THR2), 1)) { alpha = 1.f; }
;     else { const float dl = first ? u : fmaxf(u, 0.f); alpha = __builtin_amdgcn_exp2f(-dl); m_reg += dl;
; #pragma unroll
;         for (int r = 0; r < 16; ++r) { p0[r] -= dl; p1[r] -= dl; } }
; #pragma unroll
;     for (int r = 0; r < 16; ++r) p0[r] = __builtin_amdgcn_exp2f(p0[r]);
; }
; __device__ __forceinline__ void finishSM(f32x16& p0, f32x16& p1, float alpha, float& l_reg, v8i& pa) {
; #pragma unroll
;     for (int r = 0; r < 16; ++r) p1[r] = __builtin_amdgcn_exp2f(p1[r]);
;     float sa = p0[0] + p0[1], sb = p0[2] + p0[3], sc = p0[4] + p0[5], sd = p0[6] + p0[7];
;     sa += p0[8]; sb += p0[9]; sc += p0[10]; sd += p0[11]; sa += p0[12]; sb += p0[13]; sc += p0[14]; sd += p0[15];
; #pragma unroll
;     for (int r = 0; r < 16; r += 4) { sa += p1[r]; sb += p1[r + 1]; sc += p1[r + 2]; sd += p1[r + 3]; }
;     float ps = (sa + sb) + (sc + sd);
;     { auto rr = __builtin_amdgcn_permlane32_swap(__float_as_uint(ps), __float_as_uint(ps), false, false);
;       ps = __uint_as_float(rr[0]) + __uint_as_float(rr[1]); }
;     l_reg = l_reg * alpha + ps;
; #pragma unroll
;     for (int c = 0; c < 4; ++c) { pa[c] = (int)pk4_fp8(p0[4 * c], p0[4 * c + 1], p0[4 * c + 2], p0[4 * c + 3]);
;         pa[4 + c] = (int)pk4_fp8(p1[4 * c], p1[4 * c + 1], p1[4 * c + 2], p1[4 * c + 3]); }
; }
; __device__ __forceinline__ void qkt(f32x16& p0, f32x16& p1, const float m_reg, const char* Ks, const v8i* q8, int r32, int hi) {
;     { const float ini = PSH - m_reg;
.LBB0_563:
	v_sub_f32_e32 v64, 0x40400000, v180
	v_mov_b32_e32 v65, v64
	v_mov_b64_e32 v[66:67], v[64:65]
	v_mov_b64_e32 v[68:69], v[64:65]
	v_mov_b64_e32 v[70:71], v[64:65]
	v_mov_b64_e32 v[72:73], v[64:65]
	v_mov_b64_e32 v[74:75], v[64:65]
	v_mov_b64_e32 v[76:77], v[64:65]
	v_mov_b64_e32 v[78:79], v[64:65]
	v_exp_f32_e32 v231, v80
	v_exp_f32_e32 v233, v81
	s_waitcnt lgkmcnt(2)
	v_mfma_scale_f32_32x32x64_f8f6f4 v[96:111], v[96:103], v[120:127], v[64:79], v201, v200 op_sel_hi:[0,0,0]
	v_exp_f32_e32 v225, v82
	v_exp_f32_e32 v226, v83
	v_exp_f32_e32 v232, v84
	v_exp_f32_e32 v234, v85
	v_exp_f32_e32 v229, v86
	v_exp_f32_e32 v230, v87
	v_add_f32_e32 v80, v216, v215
	v_add_f32_e32 v81, v194, v192
	v_add_f32_e32 v82, v214, v213
	v_add_f32_e32 v83, v212, v211
	v_exp_f32_e32 v227, v88
	v_exp_f32_e32 v228, v89
	v_exp_f32_e32 v219, v90
	v_exp_f32_e32 v220, v91
	v_add_f32_e32 v80, v193, v80
	s_waitcnt lgkmcnt(0)
	v_mfma_scale_f32_32x32x64_f8f6f4 v[64:79], v[136:143], v[120:127], v[64:79], v201, v200 op_sel_hi:[0,0,0]
	ds_read_b128 v[136:139], v164 offset:64
	ds_read_b128 v[140:143], v164 offset:80
	ds_read_b128 v[144:147], v164 offset:6720
	ds_read_b128 v[148:151], v164 offset:6736
	v_add_f32_e32 v81, v195, v81
	v_add_f32_e32 v82, v186, v82
	v_add_f32_e32 v83, v187, v83
	v_exp_f32_e32 v223, v92
	v_exp_f32_e32 v224, v93
	v_exp_f32_e32 v221, v94
	v_exp_f32_e32 v222, v95
	v_add_f32_e32 v80, v190, v80
	v_add_f32_e32 v81, v191, v81
	v_add_f32_e32 v82, v188, v82
	v_add_f32_e32 v83, v189, v83
	v_add_f32_e32 v80, v80, v231
	v_add_f32_e32 v81, v81, v233
	v_add_f32_e32 v82, v82, v225
	s_waitcnt lgkmcnt(2)
	v_mfma_scale_f32_32x32x64_f8f6f4 v[96:111], v[136:143], v[128:135], v[96:111], v201, v200 op_sel_hi:[0,0,0]
	v_add_f32_e32 v83, v83, v226
	v_add_f32_e32 v80, v232, v80
	v_add_f32_e32 v81, v234, v81
	v_add_f32_e32 v82, v229, v82
	v_add_f32_e32 v83, v230, v83
	v_add_f32_e32 v80, v227, v80
	v_add_f32_e32 v81, v228, v81
	v_add_f32_e32 v82, v219, v82
	v_add_f32_e32 v83, v220, v83
	v_add_f32_e32 v80, v223, v80
	v_add_f32_e32 v81, v224, v81
	v_add_f32_e32 v82, v221, v82
	v_add_f32_e32 v83, v222, v83
	v_add_f32_e32 v80, v81, v80
	v_add_f32_e32 v81, v82, v83
	s_waitcnt lgkmcnt(0)
	v_mfma_scale_f32_32x32x64_f8f6f4 v[64:79], v[144:151], v[128:135], v[64:79], v201, v200 op_sel_hi:[0,0,0]
	ds_read_b128 v[136:139], v164 offset:128
	ds_read_b128 v[140:143], v164 offset:144
	ds_read_b128 v[144:147], v164 offset:6784
	ds_read_b128 v[148:151], v164 offset:6800
	v_add_f32_e32 v217, v81, v80
	v_mov_b32_e32 v218, v217
	v_cvt_pk_fp8_f32 v236, v215, v216
	v_cvt_pk_fp8_f32 v240, v231, v233
	v_cvt_pk_fp8_f32 v237, v213, v214
	v_cvt_pk_fp8_f32 v241, v232, v234
	v_cvt_pk_fp8_f32 v238, v193, v195
	v_cvt_pk_fp8_f32 v242, v227, v228
	v_cvt_pk_fp8_f32 v239, v190, v191
	v_cvt_pk_fp8_f32 v243, v223, v224
	v_permlane32_swap_b32_e32 v217, v218
	s_waitcnt lgkmcnt(2)
	v_mfma_scale_f32_32x32x64_f8f6f4 v[96:111], v[136:143], v[112:119], v[96:111], v201, v200 op_sel_hi:[0,0,0]
	v_cvt_pk_fp8_f32 v236, v192, v194 op_sel:[0,0,1]
	v_cvt_pk_fp8_f32 v240, v225, v226 op_sel:[0,0,1]
	v_cvt_pk_fp8_f32 v237, v211, v212 op_sel:[0,0,1]
	v_cvt_pk_fp8_f32 v241, v229, v230 op_sel:[0,0,1]
	v_cvt_pk_fp8_f32 v238, v186, v187 op_sel:[0,0,1]
	v_cvt_pk_fp8_f32 v242, v219, v220 op_sel:[0,0,1]
	v_cvt_pk_fp8_f32 v239, v188, v189 op_sel:[0,0,1]
	v_cvt_pk_fp8_f32 v243, v221, v222 op_sel:[0,0,1]
	s_waitcnt lgkmcnt(0)
	v_mfma_scale_f32_32x32x64_f8f6f4 v[64:79], v[144:151], v[112:119], v[64:79], v201, v200 op_sel_hi:[0,0,0]
	v_add3_u32 v84, s12, v161, v179
	ds_read_b128 v[144:147], v84 offset:13312
	ds_read_b128 v[148:151], v84 offset:13328
	ds_read_b128 v[136:139], v84 offset:15872
	ds_read_b128 v[140:143], v84 offset:15888
	ds_read_b128 v[88:91], v84 offset:18432
	ds_read_b128 v[92:95], v84 offset:18448
	ds_read_b128 v[80:83], v84 offset:20992
	ds_read_b128 v[84:87], v84 offset:21008
	s_nop 2
	v_max_f32_e32 v164, v96, v97
	v_max3_f32 v165, v99, v100, v101
	v_max3_f32 v164, v164, v98, v108
	v_max3_f32 v165, v165, v110, v111
	v_max3_f32 v166, v102, v103, v104
	v_max3_f32 v167, v105, v106, v107
	s_waitcnt lgkmcnt(6)
	v_mfma_scale_f32_32x32x64_f8f6f4 v[0:15], v[236:243], v[144:151], v[0:15], v201, v201 op_sel_hi:[0,0,0]
	v_max3_f32 v164, v164, v109, v68
	v_max3_f32 v165, v165, v70, v71
	v_max3_f32 v166, v166, v64, v65
	v_max3_f32 v167, v167, v66, v67
	v_max3_f32 v164, v164, v69, v76
	v_max3_f32 v165, v165, v78, v79
	v_max3_f32 v166, v166, v72, v73
	v_max3_f32 v167, v167, v74, v75
	s_waitcnt lgkmcnt(4)
	v_mfma_scale_f32_32x32x64_f8f6f4 v[48:63], v[236:243], v[136:143], v[48:63], v201, v201 op_sel_hi:[0,0,0]
	v_max3_f32 v164, v164, v77, v165
	v_max3_f32 v164, v164, v166, v167
	s_mov_b32 s0, 0x410c551d
	v_cmp_ge_f32_e32 vcc, s0, v164
	s_cmp_eq_u64 vcc, exec
	v_mov_b32_e32 v184, 1.0
	s_cbranch_scc0 .LBB0_571
; __device__ __forceinline__ void partialSM(f32x16& p0, f32x16& p1, float& m_reg, float& alpha, const bool first) {
;     ...
;     if (__builtin_expect(!first && __all(u <= THR2), 1)) { alpha = 1.f; }
;     else { const float dl = first ? u : fmaxf(u, 0.f); alpha = __builtin_amdgcn_exp2f(-dl); m_reg += dl;
; #pragma unroll
;         for (int r = 0; r < 16; ++r) { p0[r] -= dl; p1[r] -= dl; } }
; #pragma unroll
;     for (int r = 0; r < 16; ++r) p0[r] = __builtin_amdgcn_exp2f(p0[r]);
.LBB0_564:
	s_waitcnt lgkmcnt(2)
	v_mfma_scale_f32_32x32x64_f8f6f4 v[32:47], v[236:243], v[88:95], v[32:47], v201, v201 op_sel_hi:[0,0,0]
	v_exp_f32_e32 v215, v96
	v_exp_f32_e32 v216, v97
	v_exp_f32_e32 v190, v98
	v_exp_f32_e32 v192, v99
	v_exp_f32_e32 v213, v100
	v_exp_f32_e32 v214, v101
	v_exp_f32_e32 v195, v102
	v_exp_f32_e32 v212, v103
	s_waitcnt lgkmcnt(0)
	v_mfma_scale_f32_32x32x64_f8f6f4 v[16:31], v[236:243], v[80:87], v[16:31], v201, v201 op_sel_hi:[0,0,0]
	v_cmp_gt_f32_e32 vcc, 1.0, v184
	v_exp_f32_e32 v194, v104
	v_exp_f32_e32 v211, v105
	v_exp_f32_e32 v186, v106
	v_exp_f32_e32 v187, v107
	v_exp_f32_e32 v191, v108
	v_exp_f32_e32 v193, v109
	v_exp_f32_e32 v188, v110
	v_exp_f32_e32 v189, v111
	s_cbranch_vccz .LBB0_568
	s_and_saveexec_b64 s[0:1], s[44:45]
	ds_write_b32 v174, v184 offset:128
	s_or_b64 exec, exec, s[0:1]
	s_waitcnt lgkmcnt(0)
	v_add_u32_e32 v92, s31, v173
	ds_read_b128 v[80:83], v92 offset:224
	ds_read_b128 v[84:87], v92 offset:192
	ds_read_b128 v[88:91], v92 offset:160
	ds_read_b128 v[92:95], v92 offset:128
	s_waitcnt lgkmcnt(0)
	s_nop 6
	v_pk_mul_f32 v[12:13], v[12:13], v[80:81]
	v_pk_mul_f32 v[8:9], v[8:9], v[84:85]
	v_pk_mul_f32 v[4:5], v[4:5], v[88:89]
	v_pk_mul_f32 v[14:15], v[14:15], v[82:83]
	v_pk_mul_f32 v[10:11], v[10:11], v[86:87]
	v_pk_mul_f32 v[6:7], v[6:7], v[90:91]
	v_pk_mul_f32 v[2:3], v[2:3], v[94:95]
	v_pk_mul_f32 v[0:1], v[0:1], v[92:93]
	v_pk_mul_f32 v[60:61], v[60:61], v[80:81]
	v_pk_mul_f32 v[56:57], v[56:57], v[84:85]
	v_pk_mul_f32 v[52:53], v[52:53], v[88:89]
	v_pk_mul_f32 v[62:63], v[62:63], v[82:83]
	v_pk_mul_f32 v[58:59], v[58:59], v[86:87]
	v_pk_mul_f32 v[54:55], v[54:55], v[90:91]
	v_pk_mul_f32 v[50:51], v[50:51], v[94:95]
	v_pk_mul_f32 v[48:49], v[48:49], v[92:93]
	v_pk_mul_f32 v[44:45], v[44:45], v[80:81]
	v_pk_mul_f32 v[40:41], v[40:41], v[84:85]
	v_pk_mul_f32 v[36:37], v[36:37], v[88:89]
	v_pk_mul_f32 v[46:47], v[46:47], v[82:83]
	v_pk_mul_f32 v[42:43], v[42:43], v[86:87]
	v_pk_mul_f32 v[38:39], v[38:39], v[90:91]
	v_pk_mul_f32 v[34:35], v[34:35], v[94:95]
	v_pk_mul_f32 v[32:33], v[32:33], v[92:93]
	v_pk_mul_f32 v[28:29], v[28:29], v[80:81]
	v_pk_mul_f32 v[24:25], v[24:25], v[84:85]
	v_pk_mul_f32 v[20:21], v[20:21], v[88:89]
	v_pk_mul_f32 v[30:31], v[30:31], v[82:83]
	v_pk_mul_f32 v[26:27], v[26:27], v[86:87]
	v_pk_mul_f32 v[22:23], v[22:23], v[90:91]
	v_pk_mul_f32 v[18:19], v[18:19], v[94:95]
	v_pk_mul_f32 v[16:17], v[16:17], v[92:93]
